# baseline (speedup 1.0000x reference)
.LBB3_9:
	ds_read_b128 v[0:3], v58
	ds_read_b128 v[28:31], v58 offset:16
	v_cmp_eq_u32_e64 s[2:3], v61, v51
	v_cmp_lt_u32_e64 s[4:5], 2, v59
	v_cmp_lt_u32_e64 s[6:7], 3, v59
	s_waitcnt lgkmcnt(1)
	v_lshl_or_b32 v1, v1, 8, v47
	v_lshl_or_b32 v0, v0, 8, v47
	v_cndmask_b32_e64 v1, v1, v63, s[2:3]
	buffer_load_dwordx4 v[24:27], v0, s[16:19], 0 offen
	buffer_load_dwordx4 v[20:23], v1, s[16:19], 0 offen
	v_lshl_or_b32 v0, v2, 8, v47
	v_lshl_or_b32 v1, v3, 8, v47
	v_cndmask_b32_e64 v0, v63, v0, s[4:5]
	v_cndmask_b32_e64 v1, v63, v1, s[6:7]
	buffer_load_dwordx4 v[16:19], v0, s[16:19], 0 offen
	buffer_load_dwordx4 v[8:11], v1, s[16:19], 0 offen
	s_waitcnt lgkmcnt(0)
	v_lshl_or_b32 v0, v28, 8, v47
	v_cmp_lt_u32_e64 s[8:9], 4, v59
	v_lshl_or_b32 v1, v29, 8, v47
	v_cmp_lt_u32_e64 s[10:11], 5, v59
	v_cndmask_b32_e64 v0, v63, v0, s[8:9]
	v_lshl_or_b32 v12, v30, 8, v47
	v_cndmask_b32_e64 v1, v63, v1, s[10:11]
	buffer_load_dwordx4 v[4:7], v0, s[16:19], 0 offen
	s_nop 0
	buffer_load_dwordx4 v[0:3], v1, s[16:19], 0 offen
	v_cmp_lt_u32_e64 s[12:13], 6, v59
	v_lshl_or_b32 v28, v31, 8, v47
	v_cmp_lt_u32_e64 s[14:15], 7, v59
	v_cndmask_b32_e64 v12, v63, v12, s[12:13]
	buffer_load_dwordx4 v[12:15], v12, s[16:19], 0 offen
	v_cndmask_b32_e64 v28, v63, v28, s[14:15]
	buffer_load_dwordx4 v[28:31], v28, s[16:19], 0 offen
	v_mov_b32_e32 v40, v41
	v_mov_b32_e32 v66, v41
	v_mov_b32_e32 v67, v41
	v_mov_b32_e32 v68, v41
	v_mov_b32_e32 v69, v41
	v_mov_b32_e32 v70, v41
	v_mov_b32_e32 v71, v41
	s_waitcnt vmcnt(7)
	v_dot2c_f32_f16_e32 v40, v24, v53
	v_dot2c_f32_f16_e32 v40, v25, v54
	s_waitcnt vmcnt(6)
	v_dot2c_f32_f16_e32 v66, v20, v53
	v_dot2c_f32_f16_e32 v40, v26, v55
	v_dot2c_f32_f16_e32 v66, v21, v54
	s_waitcnt vmcnt(5)
	v_dot2c_f32_f16_e32 v67, v16, v53
	s_waitcnt vmcnt(4)
	v_dot2c_f32_f16_e32 v68, v8, v53
	v_dot2c_f32_f16_e32 v67, v17, v54
	v_dot2c_f32_f16_e32 v68, v9, v54
	v_dot2c_f32_f16_e32 v40, v27, v56
	v_dot2c_f32_f16_e32 v66, v22, v55
	v_dot2c_f32_f16_e32 v67, v18, v55
	v_dot2c_f32_f16_e32 v68, v10, v55
	s_waitcnt vmcnt(3)
	v_dot2c_f32_f16_e32 v69, v4, v53
	s_waitcnt vmcnt(2)
	v_dot2c_f32_f16_e32 v70, v0, v53
	v_dot2c_f32_f16_e32 v69, v5, v54
	v_dot2c_f32_f16_e32 v70, v1, v54
	v_dot2c_f32_f16_e32 v69, v6, v55
	v_dot2c_f32_f16_e32 v70, v2, v55
	v_add_f32_dpp v40, v40, v40 quad_perm:[1,0,3,2] row_mask:0xf bank_mask:0xf bound_ctrl:1
	v_dot2c_f32_f16_e32 v66, v23, v56
	v_dot2c_f32_f16_e32 v67, v19, v56
	v_dot2c_f32_f16_e32 v68, v11, v56
	v_dot2c_f32_f16_e32 v69, v7, v56
	v_dot2c_f32_f16_e32 v70, v3, v56
	s_waitcnt vmcnt(1)
	v_dot2c_f32_f16_e32 v71, v12, v53
	v_add_f32_dpp v40, v40, v40 quad_perm:[2,3,0,1] row_mask:0xf bank_mask:0xf bound_ctrl:1
	v_add_f32_dpp v66, v66, v66 quad_perm:[1,0,3,2] row_mask:0xf bank_mask:0xf bound_ctrl:1
	v_add_f32_dpp v67, v67, v67 quad_perm:[1,0,3,2] row_mask:0xf bank_mask:0xf bound_ctrl:1
	v_add_f32_dpp v68, v68, v68 quad_perm:[1,0,3,2] row_mask:0xf bank_mask:0xf bound_ctrl:1
	v_add_f32_dpp v69, v69, v69 quad_perm:[1,0,3,2] row_mask:0xf bank_mask:0xf bound_ctrl:1
	v_add_f32_dpp v70, v70, v70 quad_perm:[1,0,3,2] row_mask:0xf bank_mask:0xf bound_ctrl:1
	v_dot2c_f32_f16_e32 v71, v13, v54
	v_add_f32_e32 v40, v50, v40
	v_add_f32_dpp v66, v66, v66 quad_perm:[2,3,0,1] row_mask:0xf bank_mask:0xf bound_ctrl:1
	v_add_f32_dpp v67, v67, v67 quad_perm:[2,3,0,1] row_mask:0xf bank_mask:0xf bound_ctrl:1
	v_add_f32_dpp v68, v68, v68 quad_perm:[2,3,0,1] row_mask:0xf bank_mask:0xf bound_ctrl:1
	v_add_f32_dpp v69, v69, v69 quad_perm:[2,3,0,1] row_mask:0xf bank_mask:0xf bound_ctrl:1
	v_add_f32_dpp v70, v70, v70 quad_perm:[2,3,0,1] row_mask:0xf bank_mask:0xf bound_ctrl:1
	v_dot2c_f32_f16_e32 v71, v14, v55
	v_mul_f32_e32 v72, 0x3e4ccccd, v40
	v_add_f32_e32 v66, v50, v66
	v_add_f32_e32 v67, v50, v67
	v_add_f32_e32 v68, v50, v68
	v_add_f32_e32 v69, v50, v69
	v_add_f32_e32 v70, v50, v70
	v_dot2c_f32_f16_e32 v71, v15, v56
	v_max_f32_e32 v72, v40, v72
	v_mul_f32_e32 v40, 0x3e4ccccd, v66
	v_mul_f32_e32 v73, 0x3e4ccccd, v67
	v_mul_f32_e32 v74, 0x3e4ccccd, v68
	v_mul_f32_e32 v75, 0x3e4ccccd, v69
	v_mul_f32_e32 v76, 0x3e4ccccd, v70
	v_max_f32_e32 v40, v66, v40
	v_max_f32_e32 v66, v67, v73
	v_max_f32_e32 v67, v68, v74
	v_max_f32_e32 v68, v69, v75
	v_max_f32_e32 v69, v70, v76
	v_add_f32_dpp v70, v71, v71 quad_perm:[1,0,3,2] row_mask:0xf bank_mask:0xf bound_ctrl:1
	v_cndmask_b32_e64 v66, v62, v66, s[4:5]
	v_cndmask_b32_e64 v67, v62, v67, s[6:7]
	v_add_f32_dpp v70, v70, v70 quad_perm:[2,3,0,1] row_mask:0xf bank_mask:0xf bound_ctrl:1
	v_add_f32_e32 v70, v50, v70
	v_mul_f32_e32 v71, 0x3e4ccccd, v70
	v_max_f32_e32 v70, v70, v71
	v_mov_b32_e32 v71, v41
	s_waitcnt vmcnt(0)
	v_dot2c_f32_f16_e32 v71, v28, v53
	v_dot2c_f32_f16_e32 v71, v29, v54
	v_dot2c_f32_f16_e32 v71, v30, v55
	v_dot2c_f32_f16_e32 v71, v31, v56
	v_cndmask_b32_e64 v68, v62, v68, s[8:9]
	v_cndmask_b32_e64 v69, v62, v69, s[10:11]
	v_cndmask_b32_e64 v70, v62, v70, s[12:13]
	v_add_f32_dpp v71, v71, v71 quad_perm:[1,0,3,2] row_mask:0xf bank_mask:0xf bound_ctrl:1
	s_nop 1
	v_add_f32_dpp v71, v71, v71 quad_perm:[2,3,0,1] row_mask:0xf bank_mask:0xf bound_ctrl:1
	v_add_f32_e32 v71, v50, v71
	v_mul_f32_e32 v73, 0x3e4ccccd, v71
	v_max_f32_e32 v71, v71, v73
	v_cndmask_b32_e64 v73, v40, v62, s[2:3]
	v_max_f32_e32 v40, 0xff800000, v72
	v_max3_f32 v40, v40, v73, v66
	v_max3_f32 v40, v40, v67, v68
	v_max3_f32 v40, v40, v69, v70
	v_cndmask_b32_e64 v71, v62, v71, s[14:15]
	v_max3_f32 v40, v65, v40, v71
	v_sub_f32_e32 v65, v65, v40
	v_mul_f32_e32 v65, 0x3fb8aa3b, v65
	v_exp_f32_e32 v74, v65
	v_sub_f32_e32 v65, v72, v40
	v_mul_f32_e32 v65, 0x3fb8aa3b, v65
	v_exp_f32_e32 v72, v65
	v_sub_f32_e32 v65, v73, v40
	v_mul_f32_e32 v65, 0x3fb8aa3b, v65
	v_exp_f32_e32 v73, v65
	v_sub_f32_e32 v65, v66, v40
	v_mul_f32_e32 v65, 0x3fb8aa3b, v65
	v_exp_f32_e32 v75, v65
	v_sub_f32_e32 v65, v67, v40
	v_mul_f32_e32 v65, 0x3fb8aa3b, v65
	v_exp_f32_e32 v67, v65
	v_sub_f32_e32 v65, v68, v40
	v_mul_f32_e32 v65, 0x3fb8aa3b, v65
	v_exp_f32_e32 v68, v65
	v_sub_f32_e32 v65, v69, v40
	v_mul_f32_e32 v65, 0x3fb8aa3b, v65
	v_exp_f32_e32 v69, v65
	v_sub_f32_e32 v65, v70, v40
	v_mul_f32_e32 v65, 0x3fb8aa3b, v65
	v_exp_f32_e32 v66, v65
	v_sub_f32_e32 v65, v71, v40
	v_mul_f32_e32 v65, 0x3fb8aa3b, v65
	v_exp_f32_e32 v65, v65
	v_mul_f32_e32 v38, v74, v38
	v_mul_f32_e32 v39, v74, v39
	v_mul_f32_e32 v36, v74, v36
	v_mul_f32_e32 v37, v74, v37
	v_mul_f32_e32 v34, v74, v34
	v_mul_f32_e32 v35, v74, v35
	v_mul_f32_e32 v32, v74, v32
	v_mul_f32_e32 v33, v74, v33
	s_nop 1
	s_nop 0
	v_nop
	v_nop
	v_nop
	v_nop
	v_nop
	v_nop
	v_nop
	v_nop
	v_nop
	v_nop
	v_nop
	v_nop
	v_nop
	v_nop
	v_nop
	v_nop
	v_nop
	v_nop
	v_nop
	v_nop
	v_nop
	v_nop
	v_nop
	v_nop
	v_nop
	v_nop
	v_nop
	v_nop
	v_nop
	v_nop
	v_nop
	v_nop
	v_nop
	v_nop
	v_nop
	v_nop
	v_nop
	v_nop
	v_nop
	v_nop
	v_fma_mix_f32 v38, v24, v72, v38 op_sel:[0,0,0] op_sel_hi:[1,0,0]
	v_fma_mix_f32 v39, v24, v72, v39 op_sel:[1,0,0] op_sel_hi:[1,0,0]
	v_fma_mix_f32 v36, v25, v72, v36 op_sel:[0,0,0] op_sel_hi:[1,0,0]
	v_fma_mix_f32 v37, v25, v72, v37 op_sel:[1,0,0] op_sel_hi:[1,0,0]
	v_fma_mix_f32 v34, v26, v72, v34 op_sel:[0,0,0] op_sel_hi:[1,0,0]
	v_fma_mix_f32 v35, v26, v72, v35 op_sel:[1,0,0] op_sel_hi:[1,0,0]
	v_fma_mix_f32 v32, v27, v72, v32 op_sel:[0,0,0] op_sel_hi:[1,0,0]
	v_fma_mix_f32 v33, v27, v72, v33 op_sel:[1,0,0] op_sel_hi:[1,0,0]
	v_fmac_f32_e32 v72, v64, v74
	v_fma_mix_f32 v38, v20, v73, v38 op_sel:[0,0,0] op_sel_hi:[1,0,0]
	v_fma_mix_f32 v39, v20, v73, v39 op_sel:[1,0,0] op_sel_hi:[1,0,0]
	v_fma_mix_f32 v36, v21, v73, v36 op_sel:[0,0,0] op_sel_hi:[1,0,0]
	v_fma_mix_f32 v37, v21, v73, v37 op_sel:[1,0,0] op_sel_hi:[1,0,0]
	v_fma_mix_f32 v34, v22, v73, v34 op_sel:[0,0,0] op_sel_hi:[1,0,0]
	v_fma_mix_f32 v35, v22, v73, v35 op_sel:[1,0,0] op_sel_hi:[1,0,0]
	v_fma_mix_f32 v32, v23, v73, v32 op_sel:[0,0,0] op_sel_hi:[1,0,0]
	v_fma_mix_f32 v33, v23, v73, v33 op_sel:[1,0,0] op_sel_hi:[1,0,0]
	v_add_f32_e32 v20, v72, v73
	v_fma_mix_f32 v38, v16, v75, v38 op_sel:[0,0,0] op_sel_hi:[1,0,0]
	v_fma_mix_f32 v39, v16, v75, v39 op_sel:[1,0,0] op_sel_hi:[1,0,0]
	v_fma_mix_f32 v36, v17, v75, v36 op_sel:[0,0,0] op_sel_hi:[1,0,0]
	v_fma_mix_f32 v37, v17, v75, v37 op_sel:[1,0,0] op_sel_hi:[1,0,0]
	v_fma_mix_f32 v34, v18, v75, v34 op_sel:[0,0,0] op_sel_hi:[1,0,0]
	v_fma_mix_f32 v35, v18, v75, v35 op_sel:[1,0,0] op_sel_hi:[1,0,0]
	v_fma_mix_f32 v32, v19, v75, v32 op_sel:[0,0,0] op_sel_hi:[1,0,0]
	v_fma_mix_f32 v33, v19, v75, v33 op_sel:[1,0,0] op_sel_hi:[1,0,0]
	v_add_f32_e32 v16, v20, v75
	v_fma_mix_f32 v38, v8, v67, v38 op_sel:[0,0,0] op_sel_hi:[1,0,0]
	v_fma_mix_f32 v39, v8, v67, v39 op_sel:[1,0,0] op_sel_hi:[1,0,0]
	v_fma_mix_f32 v36, v9, v67, v36 op_sel:[0,0,0] op_sel_hi:[1,0,0]
	v_fma_mix_f32 v37, v9, v67, v37 op_sel:[1,0,0] op_sel_hi:[1,0,0]
	v_fma_mix_f32 v34, v10, v67, v34 op_sel:[0,0,0] op_sel_hi:[1,0,0]
	v_fma_mix_f32 v35, v10, v67, v35 op_sel:[1,0,0] op_sel_hi:[1,0,0]
	v_fma_mix_f32 v32, v11, v67, v32 op_sel:[0,0,0] op_sel_hi:[1,0,0]
	v_fma_mix_f32 v33, v11, v67, v33 op_sel:[1,0,0] op_sel_hi:[1,0,0]
	v_add_f32_e32 v8, v16, v67
	v_fma_mix_f32 v38, v4, v68, v38 op_sel:[0,0,0] op_sel_hi:[1,0,0]
	v_fma_mix_f32 v39, v4, v68, v39 op_sel:[1,0,0] op_sel_hi:[1,0,0]
	v_fma_mix_f32 v36, v5, v68, v36 op_sel:[0,0,0] op_sel_hi:[1,0,0]
	v_fma_mix_f32 v37, v5, v68, v37 op_sel:[1,0,0] op_sel_hi:[1,0,0]
	v_fma_mix_f32 v34, v6, v68, v34 op_sel:[0,0,0] op_sel_hi:[1,0,0]
	v_fma_mix_f32 v35, v6, v68, v35 op_sel:[1,0,0] op_sel_hi:[1,0,0]
	v_fma_mix_f32 v32, v7, v68, v32 op_sel:[0,0,0] op_sel_hi:[1,0,0]
	v_fma_mix_f32 v33, v7, v68, v33 op_sel:[1,0,0] op_sel_hi:[1,0,0]
	v_add_f32_e32 v4, v8, v68
	v_fma_mix_f32 v38, v0, v69, v38 op_sel:[0,0,0] op_sel_hi:[1,0,0]
	v_fma_mix_f32 v39, v0, v69, v39 op_sel:[1,0,0] op_sel_hi:[1,0,0]
	v_fma_mix_f32 v36, v1, v69, v36 op_sel:[0,0,0] op_sel_hi:[1,0,0]
	v_fma_mix_f32 v37, v1, v69, v37 op_sel:[1,0,0] op_sel_hi:[1,0,0]
	v_fma_mix_f32 v34, v2, v69, v34 op_sel:[0,0,0] op_sel_hi:[1,0,0]
	v_fma_mix_f32 v35, v2, v69, v35 op_sel:[1,0,0] op_sel_hi:[1,0,0]
	v_fma_mix_f32 v32, v3, v69, v32 op_sel:[0,0,0] op_sel_hi:[1,0,0]
	v_fma_mix_f32 v33, v3, v69, v33 op_sel:[1,0,0] op_sel_hi:[1,0,0]
	v_add_f32_e32 v0, v4, v69
	v_fma_mix_f32 v38, v12, v66, v38 op_sel:[0,0,0] op_sel_hi:[1,0,0]
	v_fma_mix_f32 v39, v12, v66, v39 op_sel:[1,0,0] op_sel_hi:[1,0,0]
	v_fma_mix_f32 v36, v13, v66, v36 op_sel:[0,0,0] op_sel_hi:[1,0,0]
	v_fma_mix_f32 v37, v13, v66, v37 op_sel:[1,0,0] op_sel_hi:[1,0,0]
	v_fma_mix_f32 v34, v14, v66, v34 op_sel:[0,0,0] op_sel_hi:[1,0,0]
	v_fma_mix_f32 v35, v14, v66, v35 op_sel:[1,0,0] op_sel_hi:[1,0,0]
	v_fma_mix_f32 v32, v15, v66, v32 op_sel:[0,0,0] op_sel_hi:[1,0,0]
	v_fma_mix_f32 v33, v15, v66, v33 op_sel:[1,0,0] op_sel_hi:[1,0,0]
	v_add_f32_e32 v0, v0, v66
	v_fma_mix_f32 v38, v28, v65, v38 op_sel:[0,0,0] op_sel_hi:[1,0,0]
	v_fma_mix_f32 v39, v28, v65, v39 op_sel:[1,0,0] op_sel_hi:[1,0,0]
	v_fma_mix_f32 v36, v29, v65, v36 op_sel:[0,0,0] op_sel_hi:[1,0,0]
	v_fma_mix_f32 v37, v29, v65, v37 op_sel:[1,0,0] op_sel_hi:[1,0,0]
	v_fma_mix_f32 v34, v30, v65, v34 op_sel:[0,0,0] op_sel_hi:[1,0,0]
	v_fma_mix_f32 v35, v30, v65, v35 op_sel:[1,0,0] op_sel_hi:[1,0,0]
	v_fma_mix_f32 v32, v31, v65, v32 op_sel:[0,0,0] op_sel_hi:[1,0,0]
	v_fma_mix_f32 v33, v31, v65, v33 op_sel:[1,0,0] op_sel_hi:[1,0,0]
	v_add_f32_e32 v64, v0, v65
	v_mov_b32_e32 v65, v40
	s_or_b64 exec, exec, s[34:35]
	v_cmp_lt_i32_e64 s[2:3], 8, v59
	s_and_saveexec_b64 s[34:35], s[2:3]
	s_cbranch_execz .LBB3_4
.LBB3_10:
	ds_read_b128 v[0:3], v58 offset:32
	ds_read_b128 v[66:69], v58 offset:48
	v_cmp_eq_u32_e64 s[2:3], v60, v51
	v_cmp_lt_u32_e64 s[6:7], 10, v59
	v_cmp_lt_u32_e64 s[8:9], 11, v59
	s_waitcnt lgkmcnt(1)
	v_lshl_or_b32 v0, v0, 8, v47
	v_lshl_or_b32 v1, v1, 8, v47
	v_cndmask_b32_e64 v1, v1, v63, s[2:3]
	buffer_load_dwordx4 v[28:31], v0, s[16:19], 0 offen
	buffer_load_dwordx4 v[24:27], v1, s[16:19], 0 offen
	v_lshl_or_b32 v0, v2, 8, v47
	v_cndmask_b32_e64 v0, v63, v0, s[6:7]
	v_lshl_or_b32 v1, v3, 8, v47
	v_cndmask_b32_e64 v1, v63, v1, s[8:9]
	buffer_load_dwordx4 v[20:23], v0, s[16:19], 0 offen
	buffer_load_dwordx4 v[16:19], v1, s[16:19], 0 offen
	s_waitcnt lgkmcnt(0)
	v_lshl_or_b32 v0, v66, 8, v47
	v_cmp_lt_u32_e64 s[12:13], 12, v59
	v_lshl_or_b32 v1, v67, 8, v47
	v_cmp_lt_u32_e64 s[14:15], 13, v59
	v_cndmask_b32_e64 v0, v63, v0, s[12:13]
	v_cmp_lt_u32_e64 s[4:5], 14, v59
	v_cndmask_b32_e64 v1, v63, v1, s[14:15]
	buffer_load_dwordx4 v[12:15], v0, s[16:19], 0 offen
	buffer_load_dwordx4 v[8:11], v1, s[16:19], 0 offen
	v_lshl_or_b32 v0, v68, 8, v47
	v_cndmask_b32_e64 v0, v63, v0, s[4:5]
	buffer_load_dwordx4 v[4:7], v0, s[16:19], 0 offen
	v_lshl_or_b32 v0, v69, 8, v47
	v_cmp_lt_u32_e64 s[10:11], 15, v59
	v_mov_b32_e32 v40, v41
	v_mov_b32_e32 v66, v41
	v_cndmask_b32_e64 v0, v63, v0, s[10:11]
	buffer_load_dwordx4 v[0:3], v0, s[16:19], 0 offen
	v_mov_b32_e32 v67, v41
	v_mov_b32_e32 v68, v41
	v_mov_b32_e32 v69, v41
	v_mov_b32_e32 v70, v41
	s_waitcnt vmcnt(7)
	v_dot2c_f32_f16_e32 v40, v28, v53
	v_dot2c_f32_f16_e32 v40, v29, v54
	s_waitcnt vmcnt(6)
	v_dot2c_f32_f16_e32 v66, v24, v53
	v_dot2c_f32_f16_e32 v40, v30, v55
	v_dot2c_f32_f16_e32 v66, v25, v54
	s_waitcnt vmcnt(5)
	v_dot2c_f32_f16_e32 v67, v20, v53
	v_dot2c_f32_f16_e32 v67, v21, v54
	v_dot2c_f32_f16_e32 v40, v31, v56
	v_dot2c_f32_f16_e32 v66, v26, v55
	v_dot2c_f32_f16_e32 v67, v22, v55
	v_dot2c_f32_f16_e32 v66, v27, v56
	v_add_f32_dpp v40, v40, v40 quad_perm:[1,0,3,2] row_mask:0xf bank_mask:0xf bound_ctrl:1
	v_dot2c_f32_f16_e32 v67, v23, v56
	s_waitcnt vmcnt(4)
	v_dot2c_f32_f16_e32 v68, v16, v53
	v_add_f32_dpp v40, v40, v40 quad_perm:[2,3,0,1] row_mask:0xf bank_mask:0xf bound_ctrl:1
	v_add_f32_dpp v66, v66, v66 quad_perm:[1,0,3,2] row_mask:0xf bank_mask:0xf bound_ctrl:1
	v_add_f32_dpp v67, v67, v67 quad_perm:[1,0,3,2] row_mask:0xf bank_mask:0xf bound_ctrl:1
	v_add_f32_e32 v40, v50, v40
	v_add_f32_dpp v66, v66, v66 quad_perm:[2,3,0,1] row_mask:0xf bank_mask:0xf bound_ctrl:1
	v_add_f32_dpp v67, v67, v67 quad_perm:[2,3,0,1] row_mask:0xf bank_mask:0xf bound_ctrl:1
	v_mul_f32_e32 v71, 0x3e4ccccd, v40
	v_add_f32_e32 v66, v50, v66
	v_add_f32_e32 v67, v50, v67
	v_max_f32_e32 v71, v40, v71
	v_mul_f32_e32 v40, 0x3e4ccccd, v66
	v_mul_f32_e32 v72, 0x3e4ccccd, v67
	v_max_f32_e32 v40, v66, v40
	v_max_f32_e32 v66, v67, v72
	v_mov_b32_e32 v72, v41
	v_dot2c_f32_f16_e32 v68, v17, v54
	s_waitcnt vmcnt(1)
	v_dot2c_f32_f16_e32 v72, v4, v53
	v_dot2c_f32_f16_e32 v68, v18, v55
	v_dot2c_f32_f16_e32 v72, v5, v54
	v_dot2c_f32_f16_e32 v68, v19, v56
	v_dot2c_f32_f16_e32 v72, v6, v55
	v_dot2c_f32_f16_e32 v72, v7, v56
	v_dot2c_f32_f16_e32 v69, v12, v53
	v_add_f32_dpp v68, v68, v68 quad_perm:[1,0,3,2] row_mask:0xf bank_mask:0xf bound_ctrl:1
	v_dot2c_f32_f16_e32 v70, v8, v53
	v_add_f32_dpp v72, v72, v72 quad_perm:[1,0,3,2] row_mask:0xf bank_mask:0xf bound_ctrl:1
	v_add_f32_dpp v68, v68, v68 quad_perm:[2,3,0,1] row_mask:0xf bank_mask:0xf bound_ctrl:1
	v_add_f32_e32 v68, v50, v68
	v_add_f32_dpp v72, v72, v72 quad_perm:[2,3,0,1] row_mask:0xf bank_mask:0xf bound_ctrl:1
	v_mul_f32_e32 v73, 0x3e4ccccd, v68
	v_add_f32_e32 v72, v50, v72
	v_max_f32_e32 v67, v68, v73
	v_mul_f32_e32 v73, 0x3e4ccccd, v72
	v_dot2c_f32_f16_e32 v69, v13, v54
	v_dot2c_f32_f16_e32 v70, v9, v54
	v_max_f32_e32 v72, v72, v73
	v_mov_b32_e32 v73, v41
	v_dot2c_f32_f16_e32 v69, v14, v55
	v_dot2c_f32_f16_e32 v70, v10, v55
	s_waitcnt vmcnt(0)
	v_dot2c_f32_f16_e32 v73, v0, v53
	v_dot2c_f32_f16_e32 v69, v15, v56
	v_dot2c_f32_f16_e32 v70, v11, v56
	v_dot2c_f32_f16_e32 v73, v1, v54
	v_dot2c_f32_f16_e32 v73, v2, v55
	v_add_f32_dpp v69, v69, v69 quad_perm:[1,0,3,2] row_mask:0xf bank_mask:0xf bound_ctrl:1
	v_add_f32_dpp v70, v70, v70 quad_perm:[1,0,3,2] row_mask:0xf bank_mask:0xf bound_ctrl:1
	v_dot2c_f32_f16_e32 v73, v3, v56
	v_add_f32_dpp v69, v69, v69 quad_perm:[2,3,0,1] row_mask:0xf bank_mask:0xf bound_ctrl:1
	v_add_f32_dpp v70, v70, v70 quad_perm:[2,3,0,1] row_mask:0xf bank_mask:0xf bound_ctrl:1
	v_add_f32_e32 v69, v50, v69
	v_add_f32_e32 v70, v50, v70
	v_add_f32_dpp v73, v73, v73 quad_perm:[1,0,3,2] row_mask:0xf bank_mask:0xf bound_ctrl:1
	v_mul_f32_e32 v74, 0x3e4ccccd, v69
	v_mul_f32_e32 v75, 0x3e4ccccd, v70
	v_add_f32_dpp v73, v73, v73 quad_perm:[2,3,0,1] row_mask:0xf bank_mask:0xf bound_ctrl:1
	v_max_f32_e32 v76, 0xff800000, v71
	v_max_f32_e32 v68, v69, v74
	v_max_f32_e32 v69, v70, v75
	v_cndmask_b32_e64 v70, v40, v62, s[2:3]
	v_cndmask_b32_e64 v66, v62, v66, s[6:7]
	v_add_f32_e32 v73, v50, v73
	v_cndmask_b32_e64 v67, v62, v67, s[8:9]
	v_cndmask_b32_e64 v68, v62, v68, s[12:13]
	v_max3_f32 v40, v76, v70, v66
	v_mul_f32_e32 v74, 0x3e4ccccd, v73
	v_max3_f32 v40, v40, v67, v68
	v_cndmask_b32_e64 v69, v62, v69, s[14:15]
	v_cndmask_b32_e64 v72, v62, v72, s[4:5]
	v_max_f32_e32 v73, v73, v74
	v_max3_f32 v40, v40, v69, v72
	v_cndmask_b32_e64 v73, v62, v73, s[10:11]
	v_max3_f32 v40, v65, v40, v73
	v_sub_f32_e32 v65, v65, v40
	v_mul_f32_e32 v65, 0x3fb8aa3b, v65
	v_exp_f32_e32 v74, v65
	v_sub_f32_e32 v65, v71, v40
	v_mul_f32_e32 v65, 0x3fb8aa3b, v65
	v_exp_f32_e32 v71, v65
	v_sub_f32_e32 v65, v70, v40
	v_mul_f32_e32 v65, 0x3fb8aa3b, v65
	v_exp_f32_e32 v70, v65
	v_sub_f32_e32 v65, v66, v40
	v_mul_f32_e32 v65, 0x3fb8aa3b, v65
	v_exp_f32_e32 v75, v65
	v_sub_f32_e32 v65, v67, v40
	v_mul_f32_e32 v65, 0x3fb8aa3b, v65
	v_exp_f32_e32 v67, v65
	v_sub_f32_e32 v65, v68, v40
	v_mul_f32_e32 v65, 0x3fb8aa3b, v65
	v_exp_f32_e32 v68, v65
	v_sub_f32_e32 v65, v69, v40
	v_mul_f32_e32 v65, 0x3fb8aa3b, v65
	v_exp_f32_e32 v69, v65
	v_sub_f32_e32 v65, v72, v40
	v_mul_f32_e32 v65, 0x3fb8aa3b, v65
	v_exp_f32_e32 v66, v65
	v_sub_f32_e32 v65, v73, v40
	v_mul_f32_e32 v65, 0x3fb8aa3b, v65
	v_exp_f32_e32 v65, v65
	v_mul_f32_e32 v38, v74, v38
	v_mul_f32_e32 v39, v74, v39
	v_mul_f32_e32 v36, v74, v36
	v_mul_f32_e32 v37, v74, v37
	v_mul_f32_e32 v34, v74, v34
	v_mul_f32_e32 v35, v74, v35
	v_mul_f32_e32 v32, v74, v32
	v_mul_f32_e32 v33, v74, v33
	s_nop 1
	s_nop 0
	v_nop
	v_nop
	v_nop
	v_nop
	v_nop
	v_nop
	v_nop
	v_nop
	v_nop
	v_nop
	v_nop
	v_nop
	v_nop
	v_nop
	v_nop
	v_nop
	v_nop
	v_nop
	v_nop
	v_nop
	v_nop
	v_nop
	v_nop
	v_nop
	v_nop
	v_nop
	v_nop
	v_nop
	v_nop
	v_nop
	v_nop
	v_nop
	v_nop
	v_nop
	v_nop
	v_nop
	v_nop
	v_nop
	v_nop
	v_nop
	v_fma_mix_f32 v38, v28, v71, v38 op_sel:[0,0,0] op_sel_hi:[1,0,0]
	v_fma_mix_f32 v39, v28, v71, v39 op_sel:[1,0,0] op_sel_hi:[1,0,0]
	v_fma_mix_f32 v36, v29, v71, v36 op_sel:[0,0,0] op_sel_hi:[1,0,0]
	v_fma_mix_f32 v37, v29, v71, v37 op_sel:[1,0,0] op_sel_hi:[1,0,0]
	v_fma_mix_f32 v34, v30, v71, v34 op_sel:[0,0,0] op_sel_hi:[1,0,0]
	v_fma_mix_f32 v35, v30, v71, v35 op_sel:[1,0,0] op_sel_hi:[1,0,0]
	v_fma_mix_f32 v32, v31, v71, v32 op_sel:[0,0,0] op_sel_hi:[1,0,0]
	v_fma_mix_f32 v33, v31, v71, v33 op_sel:[1,0,0] op_sel_hi:[1,0,0]
	v_fmac_f32_e32 v71, v64, v74
	v_fma_mix_f32 v38, v24, v70, v38 op_sel:[0,0,0] op_sel_hi:[1,0,0]
	v_fma_mix_f32 v39, v24, v70, v39 op_sel:[1,0,0] op_sel_hi:[1,0,0]
	v_fma_mix_f32 v36, v25, v70, v36 op_sel:[0,0,0] op_sel_hi:[1,0,0]
	v_fma_mix_f32 v37, v25, v70, v37 op_sel:[1,0,0] op_sel_hi:[1,0,0]
	v_fma_mix_f32 v34, v26, v70, v34 op_sel:[0,0,0] op_sel_hi:[1,0,0]
	v_fma_mix_f32 v35, v26, v70, v35 op_sel:[1,0,0] op_sel_hi:[1,0,0]
	v_fma_mix_f32 v32, v27, v70, v32 op_sel:[0,0,0] op_sel_hi:[1,0,0]
	v_fma_mix_f32 v33, v27, v70, v33 op_sel:[1,0,0] op_sel_hi:[1,0,0]
	v_add_f32_e32 v24, v71, v70
	v_fma_mix_f32 v38, v20, v75, v38 op_sel:[0,0,0] op_sel_hi:[1,0,0]
	v_fma_mix_f32 v39, v20, v75, v39 op_sel:[1,0,0] op_sel_hi:[1,0,0]
	v_fma_mix_f32 v36, v21, v75, v36 op_sel:[0,0,0] op_sel_hi:[1,0,0]
	v_fma_mix_f32 v37, v21, v75, v37 op_sel:[1,0,0] op_sel_hi:[1,0,0]
	v_fma_mix_f32 v34, v22, v75, v34 op_sel:[0,0,0] op_sel_hi:[1,0,0]
	v_fma_mix_f32 v35, v22, v75, v35 op_sel:[1,0,0] op_sel_hi:[1,0,0]
	v_fma_mix_f32 v32, v23, v75, v32 op_sel:[0,0,0] op_sel_hi:[1,0,0]
	v_fma_mix_f32 v33, v23, v75, v33 op_sel:[1,0,0] op_sel_hi:[1,0,0]
	v_add_f32_e32 v20, v24, v75
	v_fma_mix_f32 v38, v16, v67, v38 op_sel:[0,0,0] op_sel_hi:[1,0,0]
	v_fma_mix_f32 v39, v16, v67, v39 op_sel:[1,0,0] op_sel_hi:[1,0,0]
	v_fma_mix_f32 v36, v17, v67, v36 op_sel:[0,0,0] op_sel_hi:[1,0,0]
	v_fma_mix_f32 v37, v17, v67, v37 op_sel:[1,0,0] op_sel_hi:[1,0,0]
	v_fma_mix_f32 v34, v18, v67, v34 op_sel:[0,0,0] op_sel_hi:[1,0,0]
	v_fma_mix_f32 v35, v18, v67, v35 op_sel:[1,0,0] op_sel_hi:[1,0,0]
	v_fma_mix_f32 v32, v19, v67, v32 op_sel:[0,0,0] op_sel_hi:[1,0,0]
	v_fma_mix_f32 v33, v19, v67, v33 op_sel:[1,0,0] op_sel_hi:[1,0,0]
	v_add_f32_e32 v16, v20, v67
	v_fma_mix_f32 v38, v12, v68, v38 op_sel:[0,0,0] op_sel_hi:[1,0,0]
	v_fma_mix_f32 v39, v12, v68, v39 op_sel:[1,0,0] op_sel_hi:[1,0,0]
	v_fma_mix_f32 v36, v13, v68, v36 op_sel:[0,0,0] op_sel_hi:[1,0,0]
	v_fma_mix_f32 v37, v13, v68, v37 op_sel:[1,0,0] op_sel_hi:[1,0,0]
	v_fma_mix_f32 v34, v14, v68, v34 op_sel:[0,0,0] op_sel_hi:[1,0,0]
	v_fma_mix_f32 v35, v14, v68, v35 op_sel:[1,0,0] op_sel_hi:[1,0,0]
	v_fma_mix_f32 v32, v15, v68, v32 op_sel:[0,0,0] op_sel_hi:[1,0,0]
	v_fma_mix_f32 v33, v15, v68, v33 op_sel:[1,0,0] op_sel_hi:[1,0,0]
	v_add_f32_e32 v12, v16, v68
	v_fma_mix_f32 v38, v8, v69, v38 op_sel:[0,0,0] op_sel_hi:[1,0,0]
	v_fma_mix_f32 v39, v8, v69, v39 op_sel:[1,0,0] op_sel_hi:[1,0,0]
	v_fma_mix_f32 v36, v9, v69, v36 op_sel:[0,0,0] op_sel_hi:[1,0,0]
	v_fma_mix_f32 v37, v9, v69, v37 op_sel:[1,0,0] op_sel_hi:[1,0,0]
	v_fma_mix_f32 v34, v10, v69, v34 op_sel:[0,0,0] op_sel_hi:[1,0,0]
	v_fma_mix_f32 v35, v10, v69, v35 op_sel:[1,0,0] op_sel_hi:[1,0,0]
	v_fma_mix_f32 v32, v11, v69, v32 op_sel:[0,0,0] op_sel_hi:[1,0,0]
	v_fma_mix_f32 v33, v11, v69, v33 op_sel:[1,0,0] op_sel_hi:[1,0,0]
	v_add_f32_e32 v8, v12, v69
	v_fma_mix_f32 v38, v4, v66, v38 op_sel:[0,0,0] op_sel_hi:[1,0,0]
	v_fma_mix_f32 v39, v4, v66, v39 op_sel:[1,0,0] op_sel_hi:[1,0,0]
	v_fma_mix_f32 v36, v5, v66, v36 op_sel:[0,0,0] op_sel_hi:[1,0,0]
	v_fma_mix_f32 v37, v5, v66, v37 op_sel:[1,0,0] op_sel_hi:[1,0,0]
	v_fma_mix_f32 v34, v6, v66, v34 op_sel:[0,0,0] op_sel_hi:[1,0,0]
	v_fma_mix_f32 v35, v6, v66, v35 op_sel:[1,0,0] op_sel_hi:[1,0,0]
	v_fma_mix_f32 v32, v7, v66, v32 op_sel:[0,0,0] op_sel_hi:[1,0,0]
	v_fma_mix_f32 v33, v7, v66, v33 op_sel:[1,0,0] op_sel_hi:[1,0,0]
	v_add_f32_e32 v4, v8, v66
	v_fma_mix_f32 v38, v0, v65, v38 op_sel:[0,0,0] op_sel_hi:[1,0,0]
	v_fma_mix_f32 v39, v0, v65, v39 op_sel:[1,0,0] op_sel_hi:[1,0,0]
	v_fma_mix_f32 v36, v1, v65, v36 op_sel:[0,0,0] op_sel_hi:[1,0,0]
	v_fma_mix_f32 v37, v1, v65, v37 op_sel:[1,0,0] op_sel_hi:[1,0,0]
	v_fma_mix_f32 v34, v2, v65, v34 op_sel:[0,0,0] op_sel_hi:[1,0,0]
	v_fma_mix_f32 v35, v2, v65, v35 op_sel:[1,0,0] op_sel_hi:[1,0,0]
	v_fma_mix_f32 v32, v3, v65, v32 op_sel:[0,0,0] op_sel_hi:[1,0,0]
	v_fma_mix_f32 v33, v3, v65, v33 op_sel:[1,0,0] op_sel_hi:[1,0,0]
	v_add_f32_e32 v64, v4, v65
	v_mov_b32_e32 v65, v40
	s_branch .LBB3_4
